# static s_setprio 1 for waves 4-7 during the E3 phase (diff attention + DSA), on top of lean epilogues
# baseline (speedup 1.0000x reference)
.LBB0_994:
	s_cmp_ge_i32 s4, s90
	s_cselect_b64 s[24:25], -1, 0
	s_and_b64 s[4:5], s[24:25], s[6:7]
	s_andn2_b64 vcc, exec, s[4:5]
	s_cbranch_vccnz .LBB0_1452
	v_readlane_b32 s29, v253, 8
	s_nop 3
	s_cmp_lg_u32 s29, 0
	s_cbranch_scc0 .Lprio_skip_e3
	s_setprio 1
.Lprio_skip_e3:
	v_mov_b32_e32 v0, v1
	s_cmp_eq_u32 s38, 0
	v_mbcnt_lo_u32_b32 v0, -1, v0
	v_mbcnt_hi_u32_b32 v0, -1, v0
	v_add_u32_e32 v220, s65, v0
	s_mov_b32 s4, 0x3e4ccccd
	v_min_i32_e32 v0, 0x33f, v220
	v_add_u32_e32 v2, 0xfffffd01, v0
	v_sub_u32_e32 v0, 0x2ff, v0
	v_max_i32_e32 v0, v2, v0
	v_cmp_lt_u32_e32 vcc, 14, v0
	v_min_i32_e32 v4, 0x13f, v220
	s_movk_i32 s5, 0x2ff
	v_cndmask_b32_e64 v2, 8, 9, vcc
	v_cmp_lt_u32_e32 vcc, 26, v0
	v_add_u32_e32 v5, 0xffffff01, v4
	v_sub_u32_e32 v4, 0xff, v4
	v_cndmask_b32_e64 v3, 0, 1, vcc
	v_cmp_lt_u32_e32 vcc, 49, v0
	s_cselect_b32 s4, s4, 0x3ef1014c
	s_lshl_b32 s96, s38, 7
	v_addc_co_u32_e32 v2, vcc, v2, v3, vcc
	v_cmp_lt_u32_e32 vcc, s86, v0
	v_max_i32_e32 v4, v5, v4
	s_load_dwordx2 s[6:7], s[0:1], 0xa8
	s_waitcnt lgkmcnt(0)
	s_load_dwordx2 s[12:13], s[0:1], 0xa8
	s_waitcnt lgkmcnt(0)
	s_load_dwordx2 s[8:9], s[0:1], 16
	s_waitcnt lgkmcnt(0)
	s_load_dwordx2 s[10:11], s[0:1], 64
	s_waitcnt lgkmcnt(0)
	s_nop 0
	v_cndmask_b32_e64 v3, 0, 1, vcc
	v_cmp_lt_u32_e32 vcc, s87, v0
	s_lshl_b64 s[14:15], s[96:97], 2
	v_and_b32_e32 v221, 63, v220
	v_addc_co_u32_e32 v2, vcc, v2, v3, vcc
	v_cmp_lt_u32_e32 vcc, s60, v0
	s_add_u32 s10, s10, s14
	s_addc_u32 s11, s11, s15
	v_cndmask_b32_e64 v3, 0, 1, vcc
	v_cmp_lt_u32_e32 vcc, s61, v0
	v_lshlrev_b32_e32 v222, 2, v221
	s_load_dwordx2 s[14:15], s[0:1], 0x48
	s_waitcnt lgkmcnt(0)
	s_nop 0
	v_addc_co_u32_e32 v2, vcc, v2, v3, vcc
	v_cmp_lt_i32_e32 vcc, s5, v220
	s_movk_i32 s5, 0xff
	s_nop 0
	v_cndmask_b32_e64 v3, 0, 16, vcc
	v_cmp_lt_u32_e32 vcc, 14, v4
	s_nop 1
	v_cndmask_b32_e64 v5, 8, 9, vcc
	v_cmp_lt_u32_e32 vcc, 26, v4
	s_nop 1
	v_cndmask_b32_e64 v6, 0, 1, vcc
	v_cmp_lt_u32_e32 vcc, 49, v4
	s_nop 1
	v_addc_co_u32_e32 v5, vcc, v5, v6, vcc
	global_load_dword v6, v222, s[10:11]
	global_load_dword v7, v222, s[10:11] offset:256
	global_load_dword v8, v222, s[10:11] offset:512
	global_load_dword v9, v222, s[10:11] offset:768
	v_cmp_lt_u32_e32 vcc, s86, v4
	s_nop 1
	v_cndmask_b32_e64 v10, 0, 1, vcc
	v_cmp_lt_u32_e32 vcc, s87, v4
	s_nop 1
	v_addc_co_u32_e32 v5, vcc, v5, v10, vcc
	v_cmp_lt_u32_e32 vcc, s60, v4
	s_nop 1
	v_cndmask_b32_e64 v10, 0, 1, vcc
	v_cmp_lt_u32_e32 vcc, s61, v4
	s_nop 1
	v_addc_co_u32_e32 v5, vcc, v5, v10, vcc
	v_cmp_lt_i32_e32 vcc, s5, v220
	v_readlane_b32 s5, v254, 33
	s_nop 0
	v_cndmask_b32_e64 v10, 0, 16, vcc
	v_cmp_gt_u32_e32 vcc, 8, v0
	s_nop 1
	v_cndmask_b32_e32 v0, v2, v0, vcc
	v_add_u32_e32 v0, v0, v3
	v_mul_lo_u32 v0, v0, 28
	v_cmp_gt_u32_e32 vcc, 8, v4
	v_or_b32_e32 v2, s5, v0
	v_mov_b32_e32 v3, v1
	v_cndmask_b32_e32 v0, v5, v4, vcc
	v_add_u32_e32 v0, v0, v10
	v_mul_lo_u32 v0, v0, 28
	v_lshl_add_u64 v[2:3], v[2:3], 2, s[8:9]
	v_or_b32_e32 v4, s5, v0
	v_mov_b32_e32 v5, v1
	v_lshl_add_u64 v[4:5], v[4:5], 2, s[8:9]
	global_load_dword v3, v[2:3], off offset:32
	s_nop 0
	global_load_dword v0, v[4:5], off offset:32
	v_mov_b32_e32 v10, v1
	s_movk_i32 s5, 0x340
	v_cmp_gt_i32_e32 vcc, s5, v220
	v_readlane_b32 s5, v255, 7
	s_waitcnt vmcnt(4)
	v_mul_f32_e32 v4, v6, v7
	s_nop 1
	v_mov_b32_dpp v10, v4 row_shr:1 row_mask:0xf bank_mask:0xf
	v_fmac_f32_e32 v10, v6, v7
	v_mov_b32_e32 v6, v1
	v_lshl_add_u32 v2, v220, 2, s5
	v_add_f32_dpp v4, v10, v10 row_shr:2 row_mask:0xf bank_mask:0xf bound_ctrl:1
	s_waitcnt vmcnt(2)
	v_mul_f32_e32 v5, v8, v9
	v_add_f32_dpp v4, v4, v4 row_shr:4 row_mask:0xf bank_mask:0xf bound_ctrl:1
	s_nop 1
	v_add_f32_dpp v4, v4, v4 row_shr:8 row_mask:0xf bank_mask:0xf bound_ctrl:1
	s_nop 1
	v_mov_b32_dpp v6, v4 row_bcast:15 row_mask:0xa bank_mask:0xf
	v_add_f32_e32 v4, v4, v6
	v_mov_b32_e32 v6, v1
	s_nop 1
	v_mov_b32_dpp v6, v4 row_bcast:31 row_mask:0xc bank_mask:0xf
	v_add_f32_e32 v4, v4, v6
	s_nop 0
	v_readlane_b32 s5, v4, 63
	v_mov_b32_e32 v4, v1
	s_nop 1
	v_mov_b32_dpp v4, v5 row_shr:1 row_mask:0xf bank_mask:0xf
	v_fmac_f32_e32 v4, v8, v9
	v_mov_b32_e32 v5, v1
	s_nop 0
	v_add_f32_dpp v4, v4, v4 row_shr:2 row_mask:0xf bank_mask:0xf bound_ctrl:1
	s_nop 1
	v_add_f32_dpp v4, v4, v4 row_shr:4 row_mask:0xf bank_mask:0xf bound_ctrl:1
	s_nop 1
	v_add_f32_dpp v4, v4, v4 row_shr:8 row_mask:0xf bank_mask:0xf bound_ctrl:1
	s_nop 1
	v_mov_b32_dpp v5, v4 row_bcast:15 row_mask:0xa bank_mask:0xf
	v_add_f32_e32 v4, v4, v5
	v_mov_b32_e32 v5, v1
	s_nop 1
	v_mov_b32_dpp v5, v4 row_bcast:31 row_mask:0xc bank_mask:0xf
	v_add_f32_e32 v4, v4, v5
	s_nop 0
	v_readlane_b32 s10, v4, 63
	s_and_saveexec_b64 s[8:9], vcc
	s_cbranch_execz .LBB0_997
	s_waitcnt vmcnt(1)
	v_mul_f32_e32 v3, 0x3fb8aa3b, v3
	ds_write_b32 v2, v3

.LBB0_1452:
	s_setprio 0
	v_readlane_b32 s4, v254, 51
	s_add_i32 s4, s4, 3
	s_cmp_lt_i32 s4, s91
	s_cselect_b64 s[6:7], -1, 0
	s_and_b64 s[8:9], s[24:25], s[6:7]
	s_andn2_b64 vcc, exec, s[8:9]
	s_cbranch_vccnz .LBB0_1509
	v_readlane_b32 s8, v252, 4
	v_readlane_b32 s9, v252, 5
	s_and_b64 vcc, exec, s[8:9]
	s_mov_b64 s[8:9], 0
	s_cbranch_vccnz .LBB0_1455
	v_mov_b32_e32 v0, v1
	s_nop 0
	v_mbcnt_lo_u32_b32 v0, -1, v0
	v_mbcnt_hi_u32_b32 v0, -1, v0
	v_cmp_eq_u32_e32 vcc, 0, v0
	s_and_b64 s[8:9], vcc, exec
